# defer Y0 row writes from scan 1 to scan 3 (x-producer waves write them while idle); y-writer scan-1 stores exec-masked
# speedup vs baseline: 1.0216x; 1.0216x over previous
.LBB1_35:
	s_and_saveexec_b64 s[10:11], s[4:5]
	ds_write_b32 v186, v28
	s_lshl_b32 s100, s40, 9
	v_add_u32_e32 v2, s100, v186
	ds_write_b32 v2, v28 offset:1600
	s_or_b64 exec, exec, s[10:11]
	v_mov_b32_e32 v2, 0
	ds_read_b128 v[18:21], v176
	ds_read_b128 v[22:25], v176 offset:32
	ds_read_b128 v[26:29], v176 offset:64
	ds_read_b128 v[30:33], v176 offset:96
	ds_read_b128 v[114:117], v176 offset:128
	ds_read_b128 v[118:121], v176 offset:160
	ds_read_b128 v[122:125], v176 offset:192
	ds_read_b128 v[126:129], v176 offset:224
	ds_read_b128 v[130:133], v176 offset:256
	ds_read_b128 v[134:137], v176 offset:288
	ds_read_b128 v[138:141], v176 offset:320
	ds_read_b128 v[142:145], v176 offset:352
	ds_read_b128 v[146:149], v176 offset:384
	ds_read_b128 v[150:153], v176 offset:416
	ds_read_b128 v[154:157], v176 offset:448
	ds_read_b128 v[158:161], v176 offset:480
	s_waitcnt lgkmcnt(14)
	v_dot2c_f32_f16_e32 v2, v18, v18
	v_dot2c_f32_f16_e32 v2, v19, v19
	v_dot2c_f32_f16_e32 v2, v20, v20
	v_dot2c_f32_f16_e32 v2, v21, v21
	v_dot2c_f32_f16_e32 v2, v22, v22
	v_dot2c_f32_f16_e32 v2, v23, v23
	v_dot2c_f32_f16_e32 v2, v24, v24
	v_dot2c_f32_f16_e32 v2, v25, v25
	s_waitcnt lgkmcnt(13)
	v_dot2c_f32_f16_e32 v2, v26, v26
	v_dot2c_f32_f16_e32 v2, v27, v27
	v_dot2c_f32_f16_e32 v2, v28, v28
	v_dot2c_f32_f16_e32 v2, v29, v29
	s_waitcnt lgkmcnt(12)
	v_dot2c_f32_f16_e32 v2, v30, v30
	v_dot2c_f32_f16_e32 v2, v31, v31
	v_dot2c_f32_f16_e32 v2, v32, v32
	v_dot2c_f32_f16_e32 v2, v33, v33
	s_waitcnt lgkmcnt(11)
	v_dot2c_f32_f16_e32 v2, v114, v114
	v_dot2c_f32_f16_e32 v2, v115, v115
	v_dot2c_f32_f16_e32 v2, v116, v116
	v_dot2c_f32_f16_e32 v2, v117, v117
	s_waitcnt lgkmcnt(10)
	v_dot2c_f32_f16_e32 v2, v118, v118
	v_dot2c_f32_f16_e32 v2, v119, v119
	v_dot2c_f32_f16_e32 v2, v120, v120
	v_dot2c_f32_f16_e32 v2, v121, v121
	s_waitcnt lgkmcnt(9)
	v_dot2c_f32_f16_e32 v2, v122, v122
	v_dot2c_f32_f16_e32 v2, v123, v123
	v_dot2c_f32_f16_e32 v2, v124, v124
	v_dot2c_f32_f16_e32 v2, v125, v125
	s_waitcnt lgkmcnt(8)
	v_dot2c_f32_f16_e32 v2, v126, v126
	v_dot2c_f32_f16_e32 v2, v127, v127
	v_dot2c_f32_f16_e32 v2, v128, v128
	v_dot2c_f32_f16_e32 v2, v129, v129
	s_waitcnt lgkmcnt(7)
	v_dot2c_f32_f16_e32 v2, v130, v130
	v_dot2c_f32_f16_e32 v2, v131, v131
	v_dot2c_f32_f16_e32 v2, v132, v132
	v_dot2c_f32_f16_e32 v2, v133, v133
	s_waitcnt lgkmcnt(6)
	v_dot2c_f32_f16_e32 v2, v134, v134
	v_dot2c_f32_f16_e32 v2, v135, v135
	v_dot2c_f32_f16_e32 v2, v136, v136
	v_dot2c_f32_f16_e32 v2, v137, v137
	s_waitcnt lgkmcnt(5)
	v_dot2c_f32_f16_e32 v2, v138, v138
	v_dot2c_f32_f16_e32 v2, v139, v139
	v_dot2c_f32_f16_e32 v2, v140, v140
	v_dot2c_f32_f16_e32 v2, v141, v141
	s_waitcnt lgkmcnt(4)
	v_dot2c_f32_f16_e32 v2, v142, v142
	v_dot2c_f32_f16_e32 v2, v143, v143
	v_dot2c_f32_f16_e32 v2, v144, v144
	v_dot2c_f32_f16_e32 v2, v145, v145
	s_waitcnt lgkmcnt(3)
	v_dot2c_f32_f16_e32 v2, v146, v146
	v_dot2c_f32_f16_e32 v2, v147, v147
	v_dot2c_f32_f16_e32 v2, v148, v148
	v_dot2c_f32_f16_e32 v2, v149, v149
	s_waitcnt lgkmcnt(2)
	v_dot2c_f32_f16_e32 v2, v150, v150
	v_dot2c_f32_f16_e32 v2, v151, v151
	v_dot2c_f32_f16_e32 v2, v152, v152
	v_dot2c_f32_f16_e32 v2, v153, v153
	s_waitcnt lgkmcnt(1)
	v_dot2c_f32_f16_e32 v2, v154, v154
	v_dot2c_f32_f16_e32 v2, v155, v155
	v_dot2c_f32_f16_e32 v2, v156, v156
	v_dot2c_f32_f16_e32 v2, v157, v157
	s_waitcnt lgkmcnt(0)
	v_dot2c_f32_f16_e32 v2, v158, v158
	v_dot2c_f32_f16_e32 v2, v159, v159
	v_dot2c_f32_f16_e32 v2, v160, v160
	v_dot2c_f32_f16_e32 v2, v161, v161
	s_mov_b64 s[10:11], 0
	s_barrier
	s_nop 0
	ds_bpermute_b32 v3, v1, v2
	s_waitcnt lgkmcnt(0)
	v_add_f32_e32 v2, v2, v3

.LBB1_100:
	s_and_b32 s4, s99, 0xffff8000
	s_mov_b64 s[96:97], s[14:15]
	s_mov_b64 s[92:93], s[18:19]
	s_add_i32 s4, vcc_lo, s4
	s_mov_b32 s95, s5
	s_mov_b32 s89, s5
	s_mov_b32 s87, s5
	s_mov_b32 s83, s5
	s_mov_b32 s79, s5
	s_mov_b32 s77, s5
	s_mov_b32 s73, s5
	s_mov_b32 s69, s5
	s_mov_b32 s65, s5
	s_mov_b32 s63, s5
	s_mov_b32 s61, s5
	s_mov_b32 s59, s5
	s_mov_b32 s57, s5
	s_mov_b32 s55, s5
	s_mov_b32 s49, s5
	s_add_i32 s94, s4, 1
	s_add_i32 s88, s4, 2
	s_add_i32 s86, s4, 3
	s_add_i32 s82, s4, 4
	s_add_i32 s78, s4, 5
	s_add_i32 s76, s4, 6
	s_add_i32 s72, s4, 7
	s_add_i32 s68, s4, 8
	s_add_i32 s64, s4, 9
	s_add_i32 s62, s4, 10
	s_add_i32 s60, s4, 11
	s_add_i32 s58, s4, 12
	s_add_i32 s56, s4, 13
	s_add_i32 s54, s4, 14
	s_add_i32 s48, s4, 15
	v_mov_b32_e32 v1, s3
	v_lshl_add_u64 v[132:133], s[96:97], 0, v[162:163]
	v_lshl_add_u64 v[130:131], s[92:93], 0, v[162:163]
	s_lshl_b64 s[92:93], s[4:5], 10
	s_lshl_b64 s[94:95], s[94:95], 10
	s_lshl_b64 s[88:89], s[88:89], 10
	s_lshl_b64 s[86:87], s[86:87], 10
	s_lshl_b64 s[82:83], s[82:83], 10
	s_lshl_b64 s[78:79], s[78:79], 10
	s_lshl_b64 s[76:77], s[76:77], 10
	s_lshl_b64 s[72:73], s[72:73], 10
	s_lshl_b64 s[68:69], s[68:69], 10
	s_lshl_b64 s[64:65], s[64:65], 10
	s_lshl_b64 s[62:63], s[62:63], 10
	s_lshl_b64 s[60:61], s[60:61], 10
	s_lshl_b64 s[58:59], s[58:59], 10
	s_lshl_b64 s[56:57], s[56:57], 10
	s_lshl_b64 s[54:55], s[54:55], 10
	s_lshl_b64 s[48:49], s[48:49], 10
	v_lshl_add_u64 v[144:145], v[132:133], 0, s[92:93]
	v_lshl_add_u64 v[146:147], v[132:133], 0, s[94:95]
	v_lshl_add_u64 v[148:149], v[132:133], 0, s[88:89]
	v_lshl_add_u64 v[150:151], v[132:133], 0, s[86:87]
	v_lshl_add_u64 v[152:153], v[132:133], 0, s[82:83]
	v_lshl_add_u64 v[154:155], v[132:133], 0, s[78:79]
	v_lshl_add_u64 v[156:157], v[132:133], 0, s[76:77]
	v_lshl_add_u64 v[158:159], v[132:133], 0, s[72:73]
	v_lshl_add_u64 v[160:161], v[132:133], 0, s[68:69]
	v_lshl_add_u64 v[166:167], v[132:133], 0, s[64:65]
	v_lshl_add_u64 v[168:169], v[132:133], 0, s[62:63]
	v_lshl_add_u64 v[170:171], v[132:133], 0, s[60:61]
	v_lshl_add_u64 v[172:173], v[132:133], 0, s[58:59]
	v_lshl_add_u64 v[174:175], v[132:133], 0, s[56:57]
	v_lshl_add_u64 v[176:177], v[132:133], 0, s[54:55]
	v_lshl_add_u64 v[178:179], v[132:133], 0, s[48:49]
	ds_read_b128 v[132:135], v1
	ds_read_b128 v[136:139], v1 offset:16
	s_mov_b32 s53, s5
	s_mov_b32 s7, s5
	s_mov_b32 s9, s5
	s_waitcnt lgkmcnt(1)
	v_readfirstlane_b32 s52, v132
	v_readfirstlane_b32 s50, v133
	v_readfirstlane_b32 s46, v134
	v_readfirstlane_b32 s44, v135
	ds_read_b128 v[132:135], v1 offset:32
	ds_read_b128 v[140:143], v1 offset:48
	s_mov_b32 s11, s5
	s_mov_b32 s13, s5
	s_mov_b32 s27, s5
	s_mov_b32 s29, s5
	s_mov_b32 s35, s5
	s_mov_b32 s37, s5
	s_mov_b32 s39, s5
	s_waitcnt lgkmcnt(2)
	v_readfirstlane_b32 s6, v137
	v_readfirstlane_b32 s8, v138
	v_readfirstlane_b32 s10, v139
	s_waitcnt lgkmcnt(1)
	v_readfirstlane_b32 s12, v132
	v_readfirstlane_b32 s26, v133
	v_readfirstlane_b32 s28, v134
	v_readfirstlane_b32 s34, v135
	s_waitcnt lgkmcnt(0)
	v_readfirstlane_b32 s36, v140
	v_readfirstlane_b32 s38, v141
	s_mov_b32 s51, s5
	s_mov_b32 s47, s5
	s_mov_b32 s45, s5
	s_mov_b32 s31, s5
	s_mov_b32 s41, s5
	s_mov_b32 s43, s5
	s_lshl_b64 s[52:53], s[52:53], 10
	v_readfirstlane_b32 s30, v136
	v_readfirstlane_b32 s40, v142
	v_readfirstlane_b32 s42, v143
	s_lshl_b64 s[6:7], s[6:7], 10
	s_lshl_b64 s[8:9], s[8:9], 10
	s_lshl_b64 s[10:11], s[10:11], 10
	s_lshl_b64 s[12:13], s[12:13], 10
	s_lshl_b64 s[26:27], s[26:27], 10
	s_lshl_b64 s[28:29], s[28:29], 10
	s_lshl_b64 s[34:35], s[34:35], 10
	s_lshl_b64 s[36:37], s[36:37], 10
	s_lshl_b64 s[38:39], s[38:39], 10
	v_lshl_add_u64 v[180:181], v[130:131], 0, s[52:53]
	s_lshl_b64 s[50:51], s[50:51], 10
	s_lshl_b64 s[46:47], s[46:47], 10
	s_lshl_b64 s[44:45], s[44:45], 10
	s_lshl_b64 s[30:31], s[30:31], 10
	s_mov_b64 exec, 0
	s_waitcnt vmcnt(31)
	global_store_dwordx4 v[144:145], v[26:29], off nt
	s_waitcnt vmcnt(31)
	global_store_dwordx4 v[146:147], v[18:21], off nt
	s_waitcnt vmcnt(31)
	global_store_dwordx4 v[148:149], v[10:13], off nt
	s_waitcnt vmcnt(23)
	global_store_dwordx4 v[150:151], v[2:5], off nt
	global_store_dwordx4 v[152:153], v[30:33], off nt
	global_store_dwordx4 v[154:155], v[14:17], off nt
	s_waitcnt vmcnt(25)
	global_store_dwordx4 v[156:157], v[6:9], off nt
	s_waitcnt vmcnt(25)
	global_store_dwordx4 v[158:159], v[22:25], off nt
	global_store_dwordx4 v[160:161], v[58:61], off nt
	global_store_dwordx4 v[166:167], v[54:57], off nt
	global_store_dwordx4 v[168:169], v[46:49], off nt
	s_waitcnt vmcnt(28)
	global_store_dwordx4 v[170:171], v[34:37], off nt
	global_store_dwordx4 v[172:173], v[62:65], off nt
	global_store_dwordx4 v[174:175], v[50:53], off nt
	global_store_dwordx4 v[176:177], v[42:45], off nt
	s_waitcnt vmcnt(31)
	global_store_dwordx4 v[178:179], v[38:41], off nt
	s_mov_b64 exec, -1
	s_lshl_b64 s[40:41], s[40:41], 10
	s_lshl_b64 s[42:43], s[42:43], 10
	v_lshl_add_u64 v[6:7], v[130:131], 0, s[6:7]
	v_lshl_add_u64 v[8:9], v[130:131], 0, s[8:9]
	v_lshl_add_u64 v[22:23], v[130:131], 0, s[10:11]
	v_lshl_add_u64 v[34:35], v[130:131], 0, s[12:13]
	v_lshl_add_u64 v[36:37], v[130:131], 0, s[26:27]
	v_lshl_add_u64 v[38:39], v[130:131], 0, s[28:29]
	v_lshl_add_u64 v[40:41], v[130:131], 0, s[34:35]
	v_lshl_add_u64 v[42:43], v[130:131], 0, s[36:37]
	v_lshl_add_u64 v[44:45], v[130:131], 0, s[38:39]
	v_lshl_add_u64 v[182:183], v[130:131], 0, s[50:51]
	v_lshl_add_u64 v[184:185], v[130:131], 0, s[46:47]
	v_lshl_add_u64 v[186:187], v[130:131], 0, s[44:45]
	v_lshl_add_u64 v[188:189], v[130:131], 0, s[30:31]
	v_lshl_add_u64 v[132:133], v[130:131], 0, s[40:41]
	v_lshl_add_u64 v[130:131], v[130:131], 0, s[42:43]
	global_load_dwordx4 v[26:29], v[180:181], off
	global_load_dwordx4 v[18:21], v[182:183], off
	global_load_dwordx4 v[10:13], v[184:185], off
	global_load_dwordx4 v[2:5], v[186:187], off
	global_load_dwordx4 v[30:33], v[188:189], off
	global_load_dwordx4 v[14:17], v[6:7], off
	s_nop 0
	global_load_dwordx4 v[6:9], v[8:9], off
	s_nop 0
	global_load_dwordx4 v[22:25], v[22:23], off
	s_nop 0
	global_load_dwordx4 v[58:61], v[34:35], off
	global_load_dwordx4 v[54:57], v[36:37], off
	global_load_dwordx4 v[46:49], v[38:39], off
	s_nop 0
	global_load_dwordx4 v[34:37], v[40:41], off
	global_load_dwordx4 v[62:65], v[42:43], off
	global_load_dwordx4 v[50:53], v[44:45], off
	s_nop 0
	global_load_dwordx4 v[42:45], v[132:133], off
	global_load_dwordx4 v[38:41], v[130:131], off
	s_mov_b64 s[22:23], s[14:15]
	s_mov_b64 s[24:25], s[18:19]
	s_barrier
	ds_read_b128 v[130:133], v1 offset:64
	ds_read_b128 v[134:137], v1 offset:80
	ds_read_b128 v[138:141], v1 offset:96
	ds_read_b128 v[142:145], v1 offset:112
	s_mov_b32 s67, s5
	s_add_i32 s66, s4, 16
	s_add_i32 s70, s4, 17
	s_add_i32 s74, s4, 18
	s_add_i32 s80, s4, 19
	s_add_i32 s84, s4, 20
	s_add_i32 s90, s4, 21
	s_add_i32 s96, s4, 22
	s_add_i32 s92, s4, 23
	s_add_i32 s94, s4, 24
	s_add_i32 s88, s4, 25
	s_add_i32 s86, s4, 26
	s_add_i32 s82, s4, 27
	s_add_i32 s78, s4, 28
	s_add_i32 s76, s4, 29
	s_add_i32 s72, s4, 30
	s_add_i32 s4, s4, 31
	s_mov_b32 s71, s5
	s_mov_b32 s75, s5
	s_mov_b32 s81, s5
	s_mov_b32 s85, s5
	s_mov_b32 s91, s5
	s_mov_b32 s97, s5
	s_mov_b32 s93, s5
	s_mov_b32 s95, s5
	s_mov_b32 s89, s5
	s_mov_b32 s87, s5
	s_mov_b32 s83, s5
	s_mov_b32 s79, s5
	s_mov_b32 s77, s5
	s_mov_b32 s73, s5
	s_lshl_b64 s[66:67], s[66:67], 10
	s_lshl_b64 s[30:31], s[4:5], 10
	v_lshl_add_u64 v[146:147], s[22:23], 0, v[162:163]
	s_waitcnt lgkmcnt(3)
	v_readfirstlane_b32 s4, v130
	s_mov_b32 s69, s5
	s_mov_b32 s65, s5
	s_mov_b32 s63, s5
	s_mov_b32 s61, s5
	s_mov_b32 s59, s5
	s_mov_b32 s57, s5
	s_mov_b32 s55, s5
	s_mov_b32 s49, s5
	s_mov_b32 s53, s5
	s_mov_b32 s51, s5
	s_mov_b32 s47, s5
	s_mov_b32 s45, s5
	s_lshl_b64 s[70:71], s[70:71], 10
	s_lshl_b64 s[74:75], s[74:75], 10
	s_lshl_b64 s[80:81], s[80:81], 10
	s_lshl_b64 s[84:85], s[84:85], 10
	s_lshl_b64 s[90:91], s[90:91], 10
	s_lshl_b64 s[96:97], s[96:97], 10
	s_lshl_b64 s[92:93], s[92:93], 10
	s_lshl_b64 s[94:95], s[94:95], 10
	s_lshl_b64 s[88:89], s[88:89], 10
	s_lshl_b64 s[86:87], s[86:87], 10
	s_lshl_b64 s[82:83], s[82:83], 10
	s_lshl_b64 s[78:79], s[78:79], 10
	s_lshl_b64 s[76:77], s[76:77], 10
	s_lshl_b64 s[72:73], s[72:73], 10
	v_lshl_add_u64 v[148:149], s[24:25], 0, v[162:163]
	v_lshl_add_u64 v[150:151], v[146:147], 0, s[66:67]
	v_readfirstlane_b32 s68, v131
	v_readfirstlane_b32 s64, v132
	v_readfirstlane_b32 s62, v133
	s_waitcnt lgkmcnt(2)
	v_readfirstlane_b32 s60, v135
	v_readfirstlane_b32 s58, v136
	v_readfirstlane_b32 s56, v137
	s_waitcnt lgkmcnt(1)
	v_readfirstlane_b32 s54, v139
	v_readfirstlane_b32 s48, v140
	v_readfirstlane_b32 s52, v141
	s_waitcnt lgkmcnt(0)
	v_readfirstlane_b32 s50, v143
	v_readfirstlane_b32 s46, v144
	v_readfirstlane_b32 s44, v145
	s_lshl_b64 s[6:7], s[4:5], 10
	v_readfirstlane_b32 s4, v134
	v_lshl_add_u64 v[152:153], v[146:147], 0, s[70:71]
	v_lshl_add_u64 v[154:155], v[146:147], 0, s[74:75]
	v_lshl_add_u64 v[156:157], v[146:147], 0, s[80:81]
	v_lshl_add_u64 v[158:159], v[146:147], 0, s[84:85]
	v_lshl_add_u64 v[160:161], v[146:147], 0, s[90:91]
	v_lshl_add_u64 v[166:167], v[146:147], 0, s[96:97]
	v_lshl_add_u64 v[168:169], v[146:147], 0, s[92:93]
	v_lshl_add_u64 v[170:171], v[146:147], 0, s[94:95]
	v_lshl_add_u64 v[172:173], v[146:147], 0, s[88:89]
	v_lshl_add_u64 v[174:175], v[146:147], 0, s[86:87]
	v_lshl_add_u64 v[176:177], v[146:147], 0, s[82:83]
	v_lshl_add_u64 v[178:179], v[146:147], 0, s[78:79]
	v_lshl_add_u64 v[180:181], v[146:147], 0, s[76:77]
	v_lshl_add_u64 v[182:183], v[146:147], 0, s[72:73]
	v_lshl_add_u64 v[146:147], v[146:147], 0, s[30:31]
	s_mov_b64 exec, 0
	s_waitcnt vmcnt(47)
	global_store_dwordx4 v[150:151], v[78:81], off nt
	s_waitcnt vmcnt(47)
	global_store_dwordx4 v[152:153], v[74:77], off nt
	s_waitcnt vmcnt(47)
	global_store_dwordx4 v[154:155], v[70:73], off nt
	s_waitcnt vmcnt(40)
	global_store_dwordx4 v[156:157], v[66:69], off nt
	s_waitcnt vmcnt(38)
	global_store_dwordx4 v[158:159], v[118:121], off nt
	global_store_dwordx4 v[160:161], v[86:89], off nt
	s_waitcnt vmcnt(42)
	global_store_dwordx4 v[166:167], v[82:85], off nt
	s_waitcnt vmcnt(42)
	global_store_dwordx4 v[168:169], v[90:93], off nt
	s_waitcnt vmcnt(41)
	global_store_dwordx4 v[170:171], v[126:129], off nt
	global_store_dwordx4 v[172:173], v[102:105], off nt
	global_store_dwordx4 v[174:175], v[98:101], off nt
	s_waitcnt vmcnt(45)
	global_store_dwordx4 v[176:177], v[94:97], off nt
	s_waitcnt vmcnt(44)
	global_store_dwordx4 v[178:179], v[122:125], off nt
	global_store_dwordx4 v[180:181], v[110:113], off nt
	s_waitcnt vmcnt(47)
	global_store_dwordx4 v[182:183], v[106:109], off nt
	s_waitcnt vmcnt(47)
	global_store_dwordx4 v[146:147], v[114:117], off nt
	s_mov_b64 exec, -1
	s_lshl_b64 s[8:9], s[68:69], 10
	s_lshl_b64 s[10:11], s[64:65], 10
	s_lshl_b64 s[12:13], s[62:63], 10
	s_lshl_b64 s[22:23], s[60:61], 10
	s_lshl_b64 s[24:25], s[58:59], 10
	s_lshl_b64 s[26:27], s[56:57], 10
	s_lshl_b64 s[28:29], s[54:55], 10
	s_lshl_b64 s[30:31], s[48:49], 10
	s_lshl_b64 s[34:35], s[52:53], 10
	s_lshl_b64 s[36:37], s[50:51], 10
	s_lshl_b64 s[38:39], s[46:47], 10
	s_lshl_b64 s[40:41], s[44:45], 10
	v_lshl_add_u64 v[66:67], v[148:149], 0, s[6:7]
	s_lshl_b64 s[6:7], s[4:5], 10
	v_lshl_add_u64 v[82:83], v[148:149], 0, s[8:9]
	v_lshl_add_u64 v[84:85], v[148:149], 0, s[10:11]
	v_lshl_add_u64 v[86:87], v[148:149], 0, s[12:13]
	v_lshl_add_u64 v[94:95], v[148:149], 0, s[22:23]
	v_lshl_add_u64 v[96:97], v[148:149], 0, s[24:25]
	v_lshl_add_u64 v[98:99], v[148:149], 0, s[26:27]
	v_lshl_add_u64 v[106:107], v[148:149], 0, s[28:29]
	v_lshl_add_u64 v[108:109], v[148:149], 0, s[30:31]
	v_lshl_add_u64 v[110:111], v[148:149], 0, s[34:35]
	v_lshl_add_u64 v[114:115], v[148:149], 0, s[36:37]
	v_lshl_add_u64 v[116:117], v[148:149], 0, s[38:39]
	v_lshl_add_u64 v[118:119], v[148:149], 0, s[40:41]
	v_lshl_add_u64 v[120:121], v[148:149], 0, s[6:7]
	v_readfirstlane_b32 s4, v138
	global_load_dwordx4 v[78:81], v[66:67], off
	global_load_dwordx4 v[74:77], v[82:83], off
	global_load_dwordx4 v[70:73], v[84:85], off
	s_nop 0
	global_load_dwordx4 v[66:69], v[86:87], off
	s_nop 0
	global_load_dwordx4 v[86:89], v[94:95], off
	global_load_dwordx4 v[82:85], v[96:97], off
	global_load_dwordx4 v[90:93], v[98:99], off
	global_load_dwordx4 v[102:105], v[106:107], off
	s_nop 0
	global_load_dwordx4 v[98:101], v[108:109], off
	global_load_dwordx4 v[94:97], v[110:111], off
	s_nop 0
	global_load_dwordx4 v[110:113], v[114:115], off
	global_load_dwordx4 v[106:109], v[116:117], off
	s_nop 0
	global_load_dwordx4 v[114:117], v[118:119], off
	s_nop 0
	global_load_dwordx4 v[118:121], v[120:121], off
	s_lshl_b64 s[6:7], s[4:5], 10
	v_readfirstlane_b32 s4, v142
	v_lshl_add_u64 v[122:123], v[148:149], 0, s[6:7]
	s_lshl_b64 s[6:7], s[4:5], 10
	global_load_dwordx4 v[126:129], v[122:123], off
	v_lshl_add_u64 v[122:123], v[148:149], 0, s[6:7]
	global_load_dwordx4 v[122:125], v[122:123], off
	s_add_i32 vcc_hi, vcc_hi, 2
	s_addk_i32 s99, 0x2000
	s_addk_i32 s3, 0x80
	s_add_i32 vcc_lo, vcc_lo, 32
	s_cmp_gt_u32 vcc_hi, 5
	s_waitcnt vmcnt(63) expcnt(7) lgkmcnt(15)
	s_barrier
	s_cbranch_scc0 .LBB1_100
	v_mov_b32_e32 v1, 0x22634
	s_barrier
	ds_read_b32 v130, v1
	s_waitcnt lgkmcnt(0)
	v_cmp_gt_i32_e32 vcc, 1, v130
	s_cbranch_vccnz .LBB1_104

.LBB1_151:
	s_barrier
	s_add_i32 s100, s98, 0xfffe7f90
	s_add_i32 s6, s33, -5
	s_lshl_b32 s6, s6, 3
	s_add_i32 s100, s100, s6
	s_lshl_b32 s7, s6, 2
	s_add_i32 s7, s7, 0x22640
	v_mov_b32_e32 v114, s7
	ds_read_b128 v[2:5], v114 offset:0
	ds_read_b128 v[6:9], v114 offset:16
	s_waitcnt lgkmcnt(0)
	v_lshl_or_b32 v106, v2, 10, v162
	v_lshl_or_b32 v107, v3, 10, v162
	v_lshl_or_b32 v108, v4, 10, v162
	v_lshl_or_b32 v109, v5, 10, v162
	v_lshl_or_b32 v110, v6, 10, v162
	v_lshl_or_b32 v111, v7, 10, v162
	v_lshl_or_b32 v112, v8, 10, v162
	v_lshl_or_b32 v113, v9, 10, v162
	global_load_dwordx4 v[10:13], v106, s[18:19]
	global_load_dwordx4 v[14:17], v107, s[18:19]
	global_load_dwordx4 v[18:21], v108, s[18:19]
	global_load_dwordx4 v[22:25], v109, s[18:19]
	global_load_dwordx4 v[26:29], v110, s[18:19]
	global_load_dwordx4 v[30:33], v111, s[18:19]
	global_load_dwordx4 v[34:37], v112, s[18:19]
	global_load_dwordx4 v[38:41], v113, s[18:19]
	ds_read_b128 v[2:5], v114 offset:64
	ds_read_b128 v[6:9], v114 offset:80
	s_waitcnt lgkmcnt(0)
	v_lshl_or_b32 v106, v2, 10, v162
	v_lshl_or_b32 v107, v3, 10, v162
	v_lshl_or_b32 v108, v4, 10, v162
	v_lshl_or_b32 v109, v5, 10, v162
	v_lshl_or_b32 v110, v6, 10, v162
	v_lshl_or_b32 v111, v7, 10, v162
	v_lshl_or_b32 v112, v8, 10, v162
	v_lshl_or_b32 v113, v9, 10, v162
	global_load_dwordx4 v[42:45], v106, s[18:19]
	global_load_dwordx4 v[46:49], v107, s[18:19]
	global_load_dwordx4 v[50:53], v108, s[18:19]
	global_load_dwordx4 v[54:57], v109, s[18:19]
	global_load_dwordx4 v[58:61], v110, s[18:19]
	global_load_dwordx4 v[62:65], v111, s[18:19]
	global_load_dwordx4 v[66:69], v112, s[18:19]
	global_load_dwordx4 v[70:73], v113, s[18:19]
	ds_read_b128 v[2:5], v114 offset:128
	ds_read_b128 v[6:9], v114 offset:144
	s_waitcnt lgkmcnt(0)
	v_lshl_or_b32 v106, v2, 10, v162
	v_lshl_or_b32 v107, v3, 10, v162
	v_lshl_or_b32 v108, v4, 10, v162
	v_lshl_or_b32 v109, v5, 10, v162
	v_lshl_or_b32 v110, v6, 10, v162
	v_lshl_or_b32 v111, v7, 10, v162
	v_lshl_or_b32 v112, v8, 10, v162
	v_lshl_or_b32 v113, v9, 10, v162
	global_load_dwordx4 v[74:77], v106, s[18:19]
	global_load_dwordx4 v[78:81], v107, s[18:19]
	global_load_dwordx4 v[82:85], v108, s[18:19]
	global_load_dwordx4 v[86:89], v109, s[18:19]
	global_load_dwordx4 v[90:93], v110, s[18:19]
	global_load_dwordx4 v[94:97], v111, s[18:19]
	global_load_dwordx4 v[98:101], v112, s[18:19]
	global_load_dwordx4 v[102:105], v113, s[18:19]
	s_add_i32 s2, s100, 0
	s_lshl_b32 s2, s2, 10
	s_add_u32 s2, s14, s2
	s_addc_u32 s3, s15, 0
	s_add_u32 s4, s2, 0x1000
	s_addc_u32 s5, s3, 0
	s_waitcnt vmcnt(16)
	global_store_dwordx4 v162, v[10:13], s[2:3] offset:0 nt
	global_store_dwordx4 v162, v[14:17], s[2:3] offset:1024 nt
	global_store_dwordx4 v162, v[18:21], s[2:3] offset:2048 nt
	global_store_dwordx4 v162, v[22:25], s[2:3] offset:3072 nt
	global_store_dwordx4 v162, v[26:29], s[4:5] offset:0 nt
	global_store_dwordx4 v162, v[30:33], s[4:5] offset:1024 nt
	global_store_dwordx4 v162, v[34:37], s[4:5] offset:2048 nt
	global_store_dwordx4 v162, v[38:41], s[4:5] offset:3072 nt
	s_barrier
	ds_read_b128 v[2:5], v114 offset:192
	ds_read_b128 v[6:9], v114 offset:208
	s_waitcnt lgkmcnt(0)
	v_lshl_or_b32 v106, v2, 10, v162
	v_lshl_or_b32 v107, v3, 10, v162
	v_lshl_or_b32 v108, v4, 10, v162
	v_lshl_or_b32 v109, v5, 10, v162
	v_lshl_or_b32 v110, v6, 10, v162
	v_lshl_or_b32 v111, v7, 10, v162
	v_lshl_or_b32 v112, v8, 10, v162
	v_lshl_or_b32 v113, v9, 10, v162
	global_load_dwordx4 v[10:13], v106, s[18:19]
	global_load_dwordx4 v[14:17], v107, s[18:19]
	global_load_dwordx4 v[18:21], v108, s[18:19]
	global_load_dwordx4 v[22:25], v109, s[18:19]
	global_load_dwordx4 v[26:29], v110, s[18:19]
	global_load_dwordx4 v[30:33], v111, s[18:19]
	global_load_dwordx4 v[34:37], v112, s[18:19]
	global_load_dwordx4 v[38:41], v113, s[18:19]
	s_add_i32 s2, s100, 16
	s_lshl_b32 s2, s2, 10
	s_add_u32 s2, s14, s2
	s_addc_u32 s3, s15, 0
	s_add_u32 s4, s2, 0x1000
	s_addc_u32 s5, s3, 0
	s_waitcnt vmcnt(24)
	global_store_dwordx4 v162, v[42:45], s[2:3] offset:0 nt
	global_store_dwordx4 v162, v[46:49], s[2:3] offset:1024 nt
	global_store_dwordx4 v162, v[50:53], s[2:3] offset:2048 nt
	global_store_dwordx4 v162, v[54:57], s[2:3] offset:3072 nt
	global_store_dwordx4 v162, v[58:61], s[4:5] offset:0 nt
	global_store_dwordx4 v162, v[62:65], s[4:5] offset:1024 nt
	global_store_dwordx4 v162, v[66:69], s[4:5] offset:2048 nt
	global_store_dwordx4 v162, v[70:73], s[4:5] offset:3072 nt
	s_barrier
	ds_read_b128 v[2:5], v114 offset:256
	ds_read_b128 v[6:9], v114 offset:272
	s_waitcnt lgkmcnt(0)
	v_lshl_or_b32 v106, v2, 10, v162
	v_lshl_or_b32 v107, v3, 10, v162
	v_lshl_or_b32 v108, v4, 10, v162
	v_lshl_or_b32 v109, v5, 10, v162
	v_lshl_or_b32 v110, v6, 10, v162
	v_lshl_or_b32 v111, v7, 10, v162
	v_lshl_or_b32 v112, v8, 10, v162
	v_lshl_or_b32 v113, v9, 10, v162
	global_load_dwordx4 v[42:45], v106, s[18:19]
	global_load_dwordx4 v[46:49], v107, s[18:19]
	global_load_dwordx4 v[50:53], v108, s[18:19]
	global_load_dwordx4 v[54:57], v109, s[18:19]
	global_load_dwordx4 v[58:61], v110, s[18:19]
	global_load_dwordx4 v[62:65], v111, s[18:19]
	global_load_dwordx4 v[66:69], v112, s[18:19]
	global_load_dwordx4 v[70:73], v113, s[18:19]
	s_add_i32 s2, s100, 32
	s_lshl_b32 s2, s2, 10
	s_add_u32 s2, s14, s2
	s_addc_u32 s3, s15, 0
	s_add_u32 s4, s2, 0x1000
	s_addc_u32 s5, s3, 0
	s_waitcnt vmcnt(32)
	global_store_dwordx4 v162, v[74:77], s[2:3] offset:0 nt
	global_store_dwordx4 v162, v[78:81], s[2:3] offset:1024 nt
	global_store_dwordx4 v162, v[82:85], s[2:3] offset:2048 nt
	global_store_dwordx4 v162, v[86:89], s[2:3] offset:3072 nt
	global_store_dwordx4 v162, v[90:93], s[4:5] offset:0 nt
	global_store_dwordx4 v162, v[94:97], s[4:5] offset:1024 nt
	global_store_dwordx4 v162, v[98:101], s[4:5] offset:2048 nt
	global_store_dwordx4 v162, v[102:105], s[4:5] offset:3072 nt
	s_barrier
	ds_read_b128 v[2:5], v114 offset:320
	ds_read_b128 v[6:9], v114 offset:336
	s_waitcnt lgkmcnt(0)
	v_lshl_or_b32 v106, v2, 10, v162
	v_lshl_or_b32 v107, v3, 10, v162
	v_lshl_or_b32 v108, v4, 10, v162
	v_lshl_or_b32 v109, v5, 10, v162
	v_lshl_or_b32 v110, v6, 10, v162
	v_lshl_or_b32 v111, v7, 10, v162
	v_lshl_or_b32 v112, v8, 10, v162
	v_lshl_or_b32 v113, v9, 10, v162
	global_load_dwordx4 v[74:77], v106, s[18:19]
	global_load_dwordx4 v[78:81], v107, s[18:19]
	global_load_dwordx4 v[82:85], v108, s[18:19]
	global_load_dwordx4 v[86:89], v109, s[18:19]
	global_load_dwordx4 v[90:93], v110, s[18:19]
	global_load_dwordx4 v[94:97], v111, s[18:19]
	global_load_dwordx4 v[98:101], v112, s[18:19]
	global_load_dwordx4 v[102:105], v113, s[18:19]
	s_add_i32 s2, s100, 48
	s_lshl_b32 s2, s2, 10
	s_add_u32 s2, s14, s2
	s_addc_u32 s3, s15, 0
	s_add_u32 s4, s2, 0x1000
	s_addc_u32 s5, s3, 0
	s_waitcnt vmcnt(32)
	global_store_dwordx4 v162, v[10:13], s[2:3] offset:0 nt
	global_store_dwordx4 v162, v[14:17], s[2:3] offset:1024 nt
	global_store_dwordx4 v162, v[18:21], s[2:3] offset:2048 nt
	global_store_dwordx4 v162, v[22:25], s[2:3] offset:3072 nt
	global_store_dwordx4 v162, v[26:29], s[4:5] offset:0 nt
	global_store_dwordx4 v162, v[30:33], s[4:5] offset:1024 nt
	global_store_dwordx4 v162, v[34:37], s[4:5] offset:2048 nt
	global_store_dwordx4 v162, v[38:41], s[4:5] offset:3072 nt
	s_barrier
	ds_read_b128 v[2:5], v114 offset:384
	ds_read_b128 v[6:9], v114 offset:400
	s_waitcnt lgkmcnt(0)
	v_lshl_or_b32 v106, v2, 10, v162
	v_lshl_or_b32 v107, v3, 10, v162
	v_lshl_or_b32 v108, v4, 10, v162
	v_lshl_or_b32 v109, v5, 10, v162
	v_lshl_or_b32 v110, v6, 10, v162
	v_lshl_or_b32 v111, v7, 10, v162
	v_lshl_or_b32 v112, v8, 10, v162
	v_lshl_or_b32 v113, v9, 10, v162
	global_load_dwordx4 v[10:13], v106, s[18:19]
	global_load_dwordx4 v[14:17], v107, s[18:19]
	global_load_dwordx4 v[18:21], v108, s[18:19]
	global_load_dwordx4 v[22:25], v109, s[18:19]
	global_load_dwordx4 v[26:29], v110, s[18:19]
	global_load_dwordx4 v[30:33], v111, s[18:19]
	global_load_dwordx4 v[34:37], v112, s[18:19]
	global_load_dwordx4 v[38:41], v113, s[18:19]
	s_add_i32 s2, s100, 64
	s_lshl_b32 s2, s2, 10
	s_add_u32 s2, s14, s2
	s_addc_u32 s3, s15, 0
	s_add_u32 s4, s2, 0x1000
	s_addc_u32 s5, s3, 0
	s_waitcnt vmcnt(32)
	global_store_dwordx4 v162, v[42:45], s[2:3] offset:0 nt
	global_store_dwordx4 v162, v[46:49], s[2:3] offset:1024 nt
	global_store_dwordx4 v162, v[50:53], s[2:3] offset:2048 nt
	global_store_dwordx4 v162, v[54:57], s[2:3] offset:3072 nt
	global_store_dwordx4 v162, v[58:61], s[4:5] offset:0 nt
	global_store_dwordx4 v162, v[62:65], s[4:5] offset:1024 nt
	global_store_dwordx4 v162, v[66:69], s[4:5] offset:2048 nt
	global_store_dwordx4 v162, v[70:73], s[4:5] offset:3072 nt
	s_barrier
	ds_read_b128 v[2:5], v114 offset:448
	ds_read_b128 v[6:9], v114 offset:464
	s_waitcnt lgkmcnt(0)
	v_lshl_or_b32 v106, v2, 10, v162
	v_lshl_or_b32 v107, v3, 10, v162
	v_lshl_or_b32 v108, v4, 10, v162
	v_lshl_or_b32 v109, v5, 10, v162
	v_lshl_or_b32 v110, v6, 10, v162
	v_lshl_or_b32 v111, v7, 10, v162
	v_lshl_or_b32 v112, v8, 10, v162
	v_lshl_or_b32 v113, v9, 10, v162
	global_load_dwordx4 v[42:45], v106, s[18:19]
	global_load_dwordx4 v[46:49], v107, s[18:19]
	global_load_dwordx4 v[50:53], v108, s[18:19]
	global_load_dwordx4 v[54:57], v109, s[18:19]
	global_load_dwordx4 v[58:61], v110, s[18:19]
	global_load_dwordx4 v[62:65], v111, s[18:19]
	global_load_dwordx4 v[66:69], v112, s[18:19]
	global_load_dwordx4 v[70:73], v113, s[18:19]
	s_add_i32 s2, s100, 80
	s_lshl_b32 s2, s2, 10
	s_add_u32 s2, s14, s2
	s_addc_u32 s3, s15, 0
	s_add_u32 s4, s2, 0x1000
	s_addc_u32 s5, s3, 0
	s_waitcnt vmcnt(32)
	global_store_dwordx4 v162, v[74:77], s[2:3] offset:0 nt
	global_store_dwordx4 v162, v[78:81], s[2:3] offset:1024 nt
	global_store_dwordx4 v162, v[82:85], s[2:3] offset:2048 nt
	global_store_dwordx4 v162, v[86:89], s[2:3] offset:3072 nt
	global_store_dwordx4 v162, v[90:93], s[4:5] offset:0 nt
	global_store_dwordx4 v162, v[94:97], s[4:5] offset:1024 nt
	global_store_dwordx4 v162, v[98:101], s[4:5] offset:2048 nt
	global_store_dwordx4 v162, v[102:105], s[4:5] offset:3072 nt
	s_barrier
	s_add_i32 s2, s100, 96
	s_lshl_b32 s2, s2, 10
	s_add_u32 s2, s14, s2
	s_addc_u32 s3, s15, 0
	s_add_u32 s4, s2, 0x1000
	s_addc_u32 s5, s3, 0
	s_waitcnt vmcnt(24)
	global_store_dwordx4 v162, v[10:13], s[2:3] offset:0 nt
	global_store_dwordx4 v162, v[14:17], s[2:3] offset:1024 nt
	global_store_dwordx4 v162, v[18:21], s[2:3] offset:2048 nt
	global_store_dwordx4 v162, v[22:25], s[2:3] offset:3072 nt
	global_store_dwordx4 v162, v[26:29], s[4:5] offset:0 nt
	global_store_dwordx4 v162, v[30:33], s[4:5] offset:1024 nt
	global_store_dwordx4 v162, v[34:37], s[4:5] offset:2048 nt
	global_store_dwordx4 v162, v[38:41], s[4:5] offset:3072 nt
	s_barrier
	s_add_i32 s2, s100, 112
	s_lshl_b32 s2, s2, 10
	s_add_u32 s2, s14, s2
	s_addc_u32 s3, s15, 0
	s_add_u32 s4, s2, 0x1000
	s_addc_u32 s5, s3, 0
	s_waitcnt vmcnt(16)
	global_store_dwordx4 v162, v[42:45], s[2:3] offset:0 nt
	global_store_dwordx4 v162, v[46:49], s[2:3] offset:1024 nt
	global_store_dwordx4 v162, v[50:53], s[2:3] offset:2048 nt
	global_store_dwordx4 v162, v[54:57], s[2:3] offset:3072 nt
	global_store_dwordx4 v162, v[58:61], s[4:5] offset:0 nt
	global_store_dwordx4 v162, v[62:65], s[4:5] offset:1024 nt
	global_store_dwordx4 v162, v[66:69], s[4:5] offset:2048 nt
	global_store_dwordx4 v162, v[70:73], s[4:5] offset:3072 nt
	s_barrier
	s_barrier
	ds_read_b32 v1, v1
	s_waitcnt lgkmcnt(0)
	v_cmp_gt_i32_e32 vcc, 1, v1
	s_cbranch_vccnz .LBB1_154

.LBB1_157:
	s_waitcnt vmcnt(0)
	s_barrier
	ds_read_b32 v1, v1
	s_waitcnt lgkmcnt(0)
	v_cmp_ge_i32_e32 vcc, s33, v1
	v_readfirstlane_b32 s10, v1
	s_cbranch_vccnz .LBB1_169
	s_waitcnt vmcnt(2)
	v_cvt_f64_f32_e32 v[20:21], v2
	v_cvt_f64_f32_e32 v[18:19], v14
	v_fma_f64 v[22:23], -2.0, v[18:19], v[20:21]
	v_mul_f64 v[22:23], v[22:23], v[20:21]
	v_cvt_f64_f32_e32 v[20:21], v3
	v_cvt_f64_f32_e32 v[14:15], v15
	v_mbcnt_lo_u32_b32 v1, -1, 0
	v_fma_f64 v[24:25], -2.0, v[14:15], v[20:21]
	v_mbcnt_hi_u32_b32 v34, -1, v1
	v_fmac_f64_e32 v[22:23], v[20:21], v[24:25]
	v_cvt_f64_f32_e32 v[24:25], v4
	v_cvt_f64_f32_e32 v[20:21], v16
	v_and_b32_e32 v1, 64, v34
	v_fma_f64 v[26:27], -2.0, v[20:21], v[24:25]
	v_add_u32_e32 v35, 64, v1
	v_xor_b32_e32 v1, 32, v34
	v_fmac_f64_e32 v[22:23], v[24:25], v[26:27]
	v_cvt_f64_f32_e32 v[24:25], v5
	v_cvt_f64_f32_e32 v[16:17], v17
	v_cmp_lt_i32_e32 vcc, v1, v35
	v_fma_f64 v[26:27], -2.0, v[16:17], v[24:25]
	v_fmac_f64_e32 v[22:23], v[24:25], v[26:27]
	v_cndmask_b32_e32 v1, v34, v1, vcc
	v_lshlrev_b32_e32 v1, 2, v1
	ds_bpermute_b32 v24, v1, v22
	ds_bpermute_b32 v25, v1, v23
	v_xor_b32_e32 v32, 4, v34
	v_xor_b32_e32 v36, 1, v34
	s_waitcnt lgkmcnt(0)
	v_add_f64 v[22:23], v[22:23], v[24:25]
	v_xor_b32_e32 v24, 16, v34
	v_cmp_lt_i32_e32 vcc, v24, v35
	s_nop 1
	v_cndmask_b32_e32 v24, v34, v24, vcc
	v_lshlrev_b32_e32 v26, 2, v24
	ds_bpermute_b32 v24, v26, v22
	ds_bpermute_b32 v25, v26, v23
	s_waitcnt lgkmcnt(0)
	v_add_f64 v[22:23], v[22:23], v[24:25]
	v_xor_b32_e32 v24, 8, v34
	v_cmp_lt_i32_e32 vcc, v24, v35
	s_nop 1
	v_cndmask_b32_e32 v24, v34, v24, vcc
	v_lshlrev_b32_e32 v27, 2, v24
	ds_bpermute_b32 v24, v27, v22
	ds_bpermute_b32 v25, v27, v23
	v_cmp_lt_i32_e32 vcc, v32, v35
	s_waitcnt lgkmcnt(0)
	v_add_f64 v[22:23], v[22:23], v[24:25]
	s_waitcnt vmcnt(1)
	v_cvt_f64_f32_e32 v[24:25], v6
	v_fma_f64 v[28:29], -2.0, v[18:19], v[24:25]
	v_mul_f64 v[24:25], v[28:29], v[24:25]
	v_cvt_f64_f32_e32 v[28:29], v7
	v_fma_f64 v[30:31], -2.0, v[14:15], v[28:29]
	v_fmac_f64_e32 v[24:25], v[28:29], v[30:31]
	v_cvt_f64_f32_e32 v[28:29], v8
	v_fma_f64 v[30:31], -2.0, v[20:21], v[28:29]
	v_fmac_f64_e32 v[24:25], v[28:29], v[30:31]
	v_cvt_f64_f32_e32 v[28:29], v9
	v_fma_f64 v[30:31], -2.0, v[16:17], v[28:29]
	v_fmac_f64_e32 v[24:25], v[28:29], v[30:31]
	ds_bpermute_b32 v30, v1, v24
	ds_bpermute_b32 v31, v1, v25
	v_cndmask_b32_e32 v28, v34, v32, vcc
	v_lshlrev_b32_e32 v28, 2, v28
	ds_bpermute_b32 v32, v28, v22
	ds_bpermute_b32 v33, v28, v23
	s_waitcnt lgkmcnt(2)
	v_add_f64 v[24:25], v[24:25], v[30:31]
	ds_bpermute_b32 v30, v26, v24
	ds_bpermute_b32 v31, v26, v25
	v_xor_b32_e32 v29, 2, v34
	v_cmp_lt_i32_e32 vcc, v29, v35
	s_waitcnt lgkmcnt(2)
	v_add_f64 v[22:23], v[22:23], v[32:33]
	s_waitcnt lgkmcnt(0)
	v_add_f64 v[24:25], v[24:25], v[30:31]
	ds_bpermute_b32 v30, v27, v24
	ds_bpermute_b32 v31, v27, v25
	v_cndmask_b32_e32 v29, v34, v29, vcc
	v_lshlrev_b32_e32 v29, 2, v29
	ds_bpermute_b32 v32, v29, v22
	ds_bpermute_b32 v33, v29, v23
	s_waitcnt lgkmcnt(2)
	v_add_f64 v[24:25], v[24:25], v[30:31]
	ds_bpermute_b32 v30, v28, v24
	ds_bpermute_b32 v31, v28, v25
	v_cmp_lt_i32_e32 vcc, v36, v35
	s_waitcnt lgkmcnt(2)
	v_add_f64 v[22:23], v[22:23], v[32:33]
	s_waitcnt lgkmcnt(0)
	v_add_f64 v[24:25], v[24:25], v[30:31]
	ds_bpermute_b32 v32, v29, v24
	ds_bpermute_b32 v33, v29, v25
	v_cndmask_b32_e32 v30, v34, v36, vcc
	v_lshlrev_b32_e32 v31, 2, v30
	ds_bpermute_b32 v34, v31, v22
	ds_bpermute_b32 v35, v31, v23
	s_waitcnt lgkmcnt(2)
	v_add_f64 v[24:25], v[24:25], v[32:33]
	ds_bpermute_b32 v32, v31, v24
	ds_bpermute_b32 v33, v31, v25
	s_waitcnt lgkmcnt(2)
	v_add_f64 v[22:23], v[22:23], v[34:35]
	s_waitcnt lgkmcnt(0)
	v_add_f64 v[24:25], v[24:25], v[32:33]
	v_cmp_lt_f64_e64 s[6:7], v[24:25], v[22:23]
	v_cmp_nlt_f64_e32 vcc, v[24:25], v[22:23]
	s_and_saveexec_b64 s[8:9], vcc
	s_cbranch_execnz .LBB1_161
	s_or_b64 exec, exec, s[8:9]
	v_mov_b32_e32 v30, s12
	s_and_saveexec_b64 s[8:9], s[6:7]
	s_cbranch_execnz .LBB1_162

	.amdhsa_kernel _Z11main_kernelPKfS0_PKDF16_S0_PfS3_
		.amdhsa_group_segment_fixed_size 142400
		.amdhsa_private_segment_fixed_size 0
		.amdhsa_kernarg_size 48
		.amdhsa_user_sgpr_count 2
		.amdhsa_user_sgpr_dispatch_ptr 0
		.amdhsa_user_sgpr_queue_ptr 0
		.amdhsa_user_sgpr_kernarg_segment_ptr 1
		.amdhsa_user_sgpr_dispatch_id 0
		.amdhsa_user_sgpr_kernarg_preload_length 0
		.amdhsa_user_sgpr_kernarg_preload_offset 0
		.amdhsa_user_sgpr_private_segment_size 0
		.amdhsa_uses_dynamic_stack 0
		.amdhsa_enable_private_segment 0
		.amdhsa_system_sgpr_workgroup_id_x 1
		.amdhsa_system_sgpr_workgroup_id_y 0
		.amdhsa_system_sgpr_workgroup_id_z 0
		.amdhsa_system_sgpr_workgroup_info 0
		.amdhsa_system_vgpr_workitem_id 0
		.amdhsa_next_free_vgpr 217
		.amdhsa_next_free_sgpr 102
		.amdhsa_accum_offset 220
		.amdhsa_reserve_vcc 1
		.amdhsa_float_round_mode_32 0
		.amdhsa_float_round_mode_16_64 0
		.amdhsa_float_denorm_mode_32 3
		.amdhsa_float_denorm_mode_16_64 3
		.amdhsa_dx10_clamp 1
		.amdhsa_ieee_mode 1
		.amdhsa_fp16_overflow 0
		.amdhsa_tg_split 0
		.amdhsa_exception_fp_ieee_invalid_op 0
		.amdhsa_exception_fp_denorm_src 0
		.amdhsa_exception_fp_ieee_div_zero 0
		.amdhsa_exception_fp_ieee_overflow 0
		.amdhsa_exception_fp_ieee_underflow 0
		.amdhsa_exception_fp_ieee_inexact 0
		.amdhsa_exception_int_div_zero 0
	.end_amdhsa_kernel

amdhsa.kernels:
  - .agpr_count:     0
    .args:
      - .actual_access:  read_only
        .address_space:  global
        .offset:         0
        .size:           8
        .value_kind:     global_buffer
      - .actual_access:  write_only
        .address_space:  global
        .offset:         8
        .size:           8
        .value_kind:     global_buffer
      - .actual_access:  write_only
        .address_space:  global
        .offset:         16
        .size:           8
        .value_kind:     global_buffer
    .group_segment_fixed_size: 0
    .kernarg_segment_align: 8
    .kernarg_segment_size: 24
    .language:       OpenCL C
    .language_version:
      - 2
      - 0
    .max_flat_workgroup_size: 256
    .name:           _Z11prep_kernelPKfPDF16_Pf
    .private_segment_fixed_size: 0
    .sgpr_count:     14
    .sgpr_spill_count: 0
    .symbol:         _Z11prep_kernelPKfPDF16_Pf.kd
    .uniform_work_group_size: 1
    .uses_dynamic_stack: false
    .vgpr_count:     20
    .vgpr_spill_count: 0
    .wavefront_size: 64
  - .agpr_count:     0
    .args:
      - .address_space:  global
        .offset:         0
        .size:           8
        .value_kind:     global_buffer
      - .address_space:  global
        .offset:         8
        .size:           8
        .value_kind:     global_buffer
      - .actual_access:  read_only
        .address_space:  global
        .offset:         16
        .size:           8
        .value_kind:     global_buffer
      - .actual_access:  read_only
        .address_space:  global
        .offset:         24
        .size:           8
        .value_kind:     global_buffer
      - .address_space:  global
        .offset:         32
        .size:           8
        .value_kind:     global_buffer
      - .address_space:  global
        .offset:         40
        .size:           8
        .value_kind:     global_buffer
    .group_segment_fixed_size: 142400
    .kernarg_segment_align: 8
    .kernarg_segment_size: 48
    .language:       OpenCL C
    .language_version:
      - 2
      - 0
    .max_flat_workgroup_size: 512
    .name:           _Z11main_kernelPKfS0_PKDF16_S0_PfS3_
    .private_segment_fixed_size: 0
    .sgpr_count:     108
    .sgpr_spill_count: 1
    .symbol:         _Z11main_kernelPKfS0_PKDF16_S0_PfS3_.kd
    .uniform_work_group_size: 1
    .uses_dynamic_stack: false
    .vgpr_count:     217
    .vgpr_spill_count: 0
    .wavefront_size: 64
